# stack of the four neutral edits: attention barrier phase shift + static prio for waves 4-7, w13 strips all loads up front, FFT wave-local pass barrier dropped
# baseline (speedup 1.0000x reference)
.LBB0_1343:
	s_and_b32 s3, s21, 3
	s_and_b64 s[4:5], exec, s[34:35]
	s_cselect_b32 s3, -1, s3
	s_cmp_eq_u32 s3, 2
	s_movk_i32 s4, 0x3080
	s_cselect_b32 s4, 0x2000, s4
	s_cmp_lg_u32 s3, 1
	s_cselect_b32 s4, s4, 0x1000
	s_cmp_gt_i32 s3, 0
	s_cselect_b32 s8, s4, 0
	s_mul_i32 s18, s8, 0xe00
	v_readlane_b32 s4, v253, 7
	v_readlane_b32 s5, v253, 8
	s_add_u32 s4, s4, s18
	v_lshlrev_b32_e32 v2, 8, v181
	v_mov_b32_e32 v3, v99
	v_lshl_add_u32 v7, v7, 7, v14
	s_addc_u32 s5, s5, 0
	v_lshlrev_b64 v[50:51], 1, v[2:3]
	v_cvt_pk_bf16_f32 v5, v5, v99
	ds_write_b16 v7, v5
	v_cvt_pk_bf16_f32 v4, v4, v99
	v_lshl_add_u64 v[2:3], s[4:5], 0, v[50:51]
	ds_write_b16 v7, v4 offset:32
	v_ashrrev_i32_e32 v4, 4, v6
	v_lshlrev_b32_e32 v5, 3, v6
	s_movk_i32 s4, 0x700
	v_and_b32_e32 v7, 0x78, v5
	v_mul_lo_u32 v8, v4, s4
	v_or_b32_e32 v8, v8, v7
	v_lshlrev_b32_e32 v52, 1, v8
	v_readfirstlane_b32 s4, v2
	v_readfirstlane_b32 s5, v3
	s_waitcnt lgkmcnt(0)
	s_barrier
	v_add_u32_e32 v54, 0x1c000, v52
	s_nop 1
	global_load_dwordx4 v[8:11], v52, s[4:5] offset:1792
	global_load_dwordx4 v[14:17], v54, s[4:5] offset:1792
	s_lshl_b32 s22, s8, 7
	v_readlane_b32 s8, v253, 5
	v_lshlrev_b32_e32 v26, 4, v6
	v_readlane_b32 s9, v253, 6
	s_add_u32 s24, s8, s22
	v_ashrrev_i32_e32 v13, 3, v6
	v_and_b32_e32 v30, 0x70, v26
	s_addc_u32 s25, s9, 0
	v_lshl_or_b32 v56, v13, 7, v30
	global_load_dwordx4 v[18:21], v52, s[4:5] offset:1536
	global_load_dwordx4 v[22:25], v54, s[4:5] offset:1536
	global_load_dwordx4 v[26:29], v56, s[24:25]
	v_lshlrev_b32_e32 v31, 7, v194
	v_lshlrev_b32_e32 v12, 1, v12
	v_readlane_b32 s4, v255, 34
	v_lshlrev_b32_e32 v32, 1, v4
	v_lshrrev_b32_e32 v33, 1, v4
	v_add3_u32 v12, s4, v31, v12
	v_and_b32_e32 v31, 0xfffff0, v4
	v_and_b32_e32 v35, 3, v4
	v_add_u32_e32 v36, 32, v4
	s_add_i32 s4, 0, 0x14000
	ds_read_b128 v[144:147], v12
	ds_read_b128 v[140:143], v12 offset:32
	ds_read_b128 v[136:139], v12 offset:64
	ds_read_b128 v[132:135], v12 offset:96
	v_and_or_b32 v12, v32, 8, v31
	v_and_or_b32 v31, v33, 4, v35
	v_and_b32_e32 v32, 0xfffff0, v36
	v_lshlrev_b32_e32 v33, 1, v36
	s_and_b64 s[0:1], s[0:1], exec
	v_bfe_u32 v34, v5, 5, 2
	v_lshrrev_b32_e32 v12, 1, v12
	v_and_or_b32 v32, v33, 8, v32
	s_cselect_b32 s5, 0x104, 4
	s_cmp_lt_u32 s3, 2
	v_lshlrev_b32_e32 v7, 1, v7
	v_or_b32_e32 v12, v12, v34
	v_lshrrev_b32_e32 v32, 1, v32
	s_cselect_b32 s3, 64, 0x42
	s_and_b64 s[0:1], exec, s[34:35]
	v_lshlrev_b32_e32 v31, 6, v31
	v_and_b32_e32 v35, 48, v7
	v_lshlrev_b32_e32 v12, 9, v12
	v_or_b32_e32 v32, v32, v34
	s_cselect_b32 s3, s5, s3
	s_add_i32 s0, 0, 0x8000
	v_lshlrev_b32_e32 v32, 9, v32
	v_or3_b32 v12, v12, v31, v35
	s_cmp_lg_u32 s0, -1
	v_or3_b32 v31, v32, v31, v35
	v_add_u32_e32 v205, 0, v12
	s_cselect_b32 s0, s0, 0
	s_movk_i32 s8, 0x70
	v_add_u32_e32 v206, 0, v31
	s_waitcnt vmcnt(0)
	v_mov_b32_e32 v12, s0
	s_movk_i32 s0, 0x180
	v_mul_lo_u32 v4, v4, s0
	v_bitop3_b32 v37, v98, v5, s8 bitop3:0x78
	s_waitcnt vmcnt(4)
	ds_write_b128 v205, v[8:11]
	s_waitcnt vmcnt(3)
	ds_write_b128 v206, v[14:17]
	v_lshrrev_b32_e32 v8, 1, v6
	v_bitop3_b32 v7, v7, v8, s8 bitop3:0x78
	v_add3_u32 v207, v7, v4, 0
	v_mul_lo_u32 v4, v13, s0
	v_or_b32_e32 v7, 0x100, v30
	v_and_b32_e32 v8, 0x70, v6
	v_mad_u32_u24 v53, v195, s0, v12
	v_xad_u32 v4, v7, v8, v4
	v_add_u32_e32 v201, v37, v53
	v_add_u32_e32 v208, 0, v4
	s_waitcnt vmcnt(2)
	ds_write_b128 v207, v[18:21] offset:32768
	s_waitcnt vmcnt(1)
	ds_write_b128 v207, v[22:25] offset:45056
	s_waitcnt vmcnt(0)
	ds_write_b128 v208, v[26:29] offset:32768
	s_waitcnt lgkmcnt(0)
	s_barrier
	ds_read_b128 v[8:11], v201
	ds_read_b128 v[12:15], v201 offset:128
	s_waitcnt lgkmcnt(1)
	v_mfma_f32_32x32x16_bf16 v[18:33], v[8:11], v[128:131], 0
	ds_read_b128 v[8:11], v201 offset:12288
	ds_read_b128 v[60:63], v201 offset:256
	v_and_b32_e32 v4, 0x70, v5
	v_bitop3_b32 v5, v98, v4, 32 bitop3:0x36
	v_add_u32_e32 v203, v5, v53
	v_bitop3_b32 v5, v98, v4, 64 bitop3:0x36
	v_add_u32_e32 v204, v5, v53
	s_waitcnt lgkmcnt(1)
	v_mfma_f32_32x32x16_bf16 v[34:49], v[8:11], v[128:131], 0
	ds_read_b128 v[8:11], v203
	ds_read_b128 v[64:67], v203 offset:128
	ds_read_b128 v[68:71], v203 offset:256
	s_movk_i32 s0, 0x60
	v_bitop3_b32 v4, v98, v4, s0 bitop3:0x36
	v_add_u32_e32 v202, v4, v53
	s_mov_b64 s[0:1], 0x38700
	v_lshl_add_u64 v[4:5], v[2:3], 0, s[0:1]
	s_waitcnt lgkmcnt(2)
	v_mfma_f32_32x32x16_bf16 v[18:33], v[8:11], v[124:127], v[18:33]
	ds_read_b128 v[8:11], v203 offset:12288
	s_mov_b64 s[0:1], 0x38600
	v_lshl_add_u64 v[2:3], v[2:3], 0, s[0:1]
	v_readfirstlane_b32 s0, v4
	v_readfirstlane_b32 s1, v5
	v_readfirstlane_b32 s8, v2
	v_readfirstlane_b32 s9, v3
	s_waitcnt lgkmcnt(0)
	v_mfma_f32_32x32x16_bf16 v[34:49], v[8:11], v[124:127], v[34:49]
	ds_read_b128 v[8:11], v204
	ds_read_b128 v[72:75], v204 offset:128
	ds_read_b128 v[76:79], v204 offset:256
	v_mov_b32_e32 v57, v99
	v_add_u32_e32 v209, 0x3000, v207
	s_cmp_lg_u32 0, -1
	v_lshlrev_b32_e32 v4, 1, v58
	v_and_b32_e32 v4, 32, v4
	s_waitcnt lgkmcnt(2)
	v_mfma_f32_32x32x16_bf16 v[18:33], v[8:11], v[120:123], v[18:33]
	ds_read_b128 v[8:11], v204 offset:12288
	s_mov_b32 s36, s63
	s_mov_b32 s37, s63
	s_mov_b32 s19, s63
	s_mov_b32 s38, s63
	s_mov_b32 s39, s63
	s_mov_b32 s40, s63
	s_waitcnt lgkmcnt(0)
	v_mfma_f32_32x32x16_bf16 v[34:49], v[8:11], v[120:123], v[34:49]
	ds_read_b128 v[8:11], v202
	ds_read_b128 v[80:83], v202 offset:128
	s_mov_b32 s41, s63
	s_mov_b32 s42, s63
	s_mov_b32 s43, s63
	s_mov_b32 s44, s63
	s_mov_b32 s45, s63
	s_mov_b32 s46, s63
	s_waitcnt lgkmcnt(1)
	v_mfma_f32_32x32x16_bf16 v[18:33], v[8:11], v[116:119], v[18:33]
	ds_read_b128 v[8:11], v202 offset:12288
	ds_read_b128 v[84:87], v202 offset:256
	s_mov_b32 s47, s63
	s_mov_b32 s48, s63
	s_mov_b32 s49, s63
	s_mov_b32 s50, s63
	s_mov_b32 s51, s63
	s_mov_b32 s23, s63
	v_mfma_f32_32x32x16_bf16 v[18:33], v[12:15], v[112:115], v[18:33]
	v_mov_b32_e32 v53, v99
	v_mov_b32_e32 v55, v99
	v_lshl_add_u64 v[182:183], s[22:23], 0, v[56:57]
	v_mov_b32_e32 v227, 0x3200
	v_mov_b32_e32 v199, 0
	s_waitcnt lgkmcnt(1)
	v_mfma_f32_32x32x16_bf16 v[34:49], v[8:11], v[116:119], v[34:49]
	ds_read_b128 v[8:11], v201 offset:12416
	ds_read_b128 v[12:15], v201 offset:12544
	v_mfma_f32_32x32x16_bf16 v[18:33], v[64:67], v[108:111], v[18:33]
	s_waitcnt lgkmcnt(1)
	v_mfma_f32_32x32x16_bf16 v[34:49], v[8:11], v[112:115], v[34:49]
	ds_read_b128 v[8:11], v203 offset:12416
	ds_read_b128 v[64:67], v203 offset:12544
	v_mfma_f32_32x32x16_bf16 v[18:33], v[72:75], v[104:107], v[18:33]
	s_waitcnt lgkmcnt(1)
	v_mfma_f32_32x32x16_bf16 v[34:49], v[8:11], v[108:111], v[34:49]
	ds_read_b128 v[8:11], v204 offset:12416
	ds_read_b128 v[72:75], v204 offset:12544
	v_mfma_f32_32x32x16_bf16 v[18:33], v[80:83], v[100:103], v[18:33]
	s_waitcnt lgkmcnt(1)
	v_mfma_f32_32x32x16_bf16 v[34:49], v[8:11], v[104:107], v[34:49]
	ds_read_b128 v[8:11], v202 offset:12416
	ds_read_b128 v[80:83], v202 offset:12544
	v_mfma_f32_32x32x16_bf16 v[18:33], v[60:63], v[144:147], v[18:33]
	global_load_dwordx4 v[60:63], v54, s[0:1]
	global_load_dwordx4 v[88:91], v52, s[8:9]
	global_load_dwordx4 v[92:95], v52, s[0:1]
	global_load_dwordx4 v[148:151], v54, s[8:9]
	s_movk_i32 s0, 0x2000
	s_mov_b32 s8, 2
	s_waitcnt lgkmcnt(1)
	v_mfma_f32_32x32x16_bf16 v[34:49], v[8:11], v[100:103], v[34:49]
	v_lshl_add_u64 v[8:9], s[24:25], 0, v[56:57]
	v_add_co_u32_e32 v2, vcc, s0, v8
	v_cmp_gt_u32_e64 s[0:1], 32, v58
	s_nop 0
	v_addc_co_u32_e32 v3, vcc, 0, v9, vcc
	global_load_dwordx4 v[152:155], v[2:3], off
	v_mfma_f32_32x32x16_bf16 v[18:33], v[68:71], v[140:143], v[18:33]
	s_waitcnt vmcnt(0)
	s_waitcnt vmcnt(2)
	ds_write_b128 v205, v[92:95] offset:16384
	ds_write_b128 v206, v[60:63] offset:16384
	ds_write_b128 v207, v[88:91] offset:57344
	s_waitcnt vmcnt(1)
	ds_write_b128 v209, v[148:151] offset:57344
	s_waitcnt vmcnt(0)
	ds_write_b128 v208, v[152:155] offset:57344
	v_mfma_f32_32x32x16_bf16 v[34:49], v[12:15], v[144:147], v[34:49]
	v_and_b32_e32 v2, 0x3fffffc0, v6
	v_lshl_add_u32 v196, v2, 2, s4
	s_cselect_b32 s4, 0, 0
	v_lshlrev_b32_e32 v3, 4, v58
	v_lshlrev_b32_e32 v2, 3, v58
	v_and_b32_e32 v3, 0xc0, v3
	v_and_or_b32 v3, v2, 24, v3
	v_mfma_f32_32x32x16_bf16 v[18:33], v[76:79], v[136:139], v[18:33]
	v_and_b32_e32 v2, 0x100, v2
	v_or3_b32 v59, v3, v4, v2
	v_mov_b64_e32 v[2:3], s[36:37]
	v_add_u32_e32 v200, s4, v59
	v_mov_b64_e32 v[16:17], s[50:51]
	v_mov_b64_e32 v[4:5], s[38:39]
	v_mov_b64_e32 v[6:7], s[40:41]
	v_mfma_f32_32x32x16_bf16 v[34:49], v[64:67], v[140:143], v[34:49]
	v_mov_b64_e32 v[8:9], s[42:43]
	v_mov_b64_e32 v[10:11], s[44:45]
	v_mov_b64_e32 v[12:13], s[46:47]
	v_mov_b64_e32 v[14:15], s[48:49]
	v_lshl_add_u32 v197, v195, 2, v196
	s_waitcnt lgkmcnt(0)
	s_barrier
	v_mfma_f32_32x32x16_bf16 v[18:33], v[84:87], v[132:135], v[18:33]
	v_mfma_f32_32x32x16_bf16 v[34:49], v[72:75], v[136:139], v[34:49]
	s_nop 10
	v_max_f32_e32 v64, v19, v19
	v_max_f32_e32 v65, v18, v18
	v_max_f32_e32 v64, v65, v64
	v_max3_f32 v64, v64, v20, v21
	v_max3_f32 v64, v64, v22, v23
	v_max3_f32 v64, v64, v24, v25
	v_max3_f32 v64, v64, v26, v27
	v_mfma_f32_32x32x16_bf16 v[34:49], v[80:83], v[132:135], v[34:49]
	v_max3_f32 v64, v64, v28, v29
	v_max3_f32 v64, v64, v30, v31
	v_max3_f32 v64, v64, v32, v33
	s_nop 8
	v_max3_f32 v64, v64, v34, v35
	v_max3_f32 v64, v64, v36, v37
	v_max3_f32 v64, v64, v38, v39
	v_max3_f32 v64, v64, v40, v41
	v_max3_f32 v64, v64, v42, v43
	v_max3_f32 v64, v64, v44, v45
	v_max3_f32 v64, v64, v46, v47
	v_max3_f32 v64, v64, v48, v49
	v_mov_b32_e32 v65, v64
	s_nop 1
	v_permlane32_swap_b32_e32 v64, v65
	v_max_f32_e32 v65, v65, v65
	v_max_f32_e32 v64, v64, v64
	v_max_f32_e32 v64, v64, v65
	v_max_f32_e32 v60, 0xf149f2ca, v64
	v_sub_f32_e32 v61, 0xf149f2ca, v60
	v_mul_f32_e32 v61, 0x3dd53b94, v61
	v_add_f32_e32 v65, 0x7149f2ca, v64
	v_exp_f32_e32 v61, v61
	v_cmp_ge_f32_e32 vcc, s11, v65
	s_cmp_eq_u64 vcc, exec
	s_cselect_b64 vcc, -1, 0
	v_cndmask_b32_e64 v210, v61, 1.0, vcc
	v_mov_b32_e32 v61, 0xf149f2ca
	v_cndmask_b32_e32 v211, v60, v61, vcc
	v_mul_f32_e32 v60, 0xbdd53b94, v211
	v_fmamk_f32 v18, v18, 0x3dd53b94, v60
	v_exp_f32_e32 v169, v18
	v_fmamk_f32 v18, v19, 0x3dd53b94, v60
	v_exp_f32_e32 v191, v18
	v_fmamk_f32 v18, v20, 0x3dd53b94, v60
	v_exp_f32_e32 v170, v18
	v_fmamk_f32 v18, v21, 0x3dd53b94, v60
	v_exp_f32_e32 v192, v18
	v_fmamk_f32 v18, v22, 0x3dd53b94, v60
	v_exp_f32_e32 v190, v18
	v_fmamk_f32 v18, v23, 0x3dd53b94, v60
	v_exp_f32_e32 v193, v18
	v_fmamk_f32 v18, v24, 0x3dd53b94, v60
	v_exp_f32_e32 v171, v18
	v_fmamk_f32 v18, v25, 0x3dd53b94, v60
	v_exp_f32_e32 v189, v18
	v_fmamk_f32 v18, v26, 0x3dd53b94, v60
	v_exp_f32_e32 v173, v18
	v_fmamk_f32 v18, v27, 0x3dd53b94, v60
	v_exp_f32_e32 v175, v18
	v_fmamk_f32 v18, v28, 0x3dd53b94, v60
	v_exp_f32_e32 v174, v18
	v_fmamk_f32 v18, v29, 0x3dd53b94, v60
	v_exp_f32_e32 v188, v18
	v_fmamk_f32 v18, v30, 0x3dd53b94, v60
	v_exp_f32_e32 v164, v18
	v_fmamk_f32 v18, v31, 0x3dd53b94, v60
	v_pk_fma_f32 v[148:149], v[48:49], s[56:57], v[60:61] op_sel_hi:[1,0,0]
	v_pk_fma_f32 v[154:155], v[46:47], s[56:57], v[60:61] op_sel_hi:[1,0,0]
	v_pk_fma_f32 v[158:159], v[44:45], s[56:57], v[60:61] op_sel_hi:[1,0,0]
	v_pk_fma_f32 v[150:151], v[42:43], s[56:57], v[60:61] op_sel_hi:[1,0,0]
	v_pk_fma_f32 v[152:153], v[40:41], s[56:57], v[60:61] op_sel_hi:[1,0,0]
	v_pk_fma_f32 v[156:157], v[38:39], s[56:57], v[60:61] op_sel_hi:[1,0,0]
	v_pk_fma_f32 v[160:161], v[36:37], s[56:57], v[60:61] op_sel_hi:[1,0,0]
	v_pk_fma_f32 v[162:163], v[34:35], s[56:57], v[60:61] op_sel_hi:[1,0,0]
	v_exp_f32_e32 v166, v18
	v_fmamk_f32 v18, v32, 0x3dd53b94, v60
	v_fmac_f32_e32 v60, 0x3dd53b94, v33
	v_exp_f32_e32 v165, v18
	v_exp_f32_e32 v167, v60
	s_addk_i32 s4, 0x4000
	v_lshl_add_u64 v[18:19], s[18:19], 0, v[50:51]
	v_add_u32_e32 v198, s4, v59
	v_lshl_add_u64 v[184:185], v[18:19], 0, v[54:55]
	v_lshl_add_u64 v[186:187], v[18:19], 0, v[52:53]
	v_mov_b64_e32 v[64:65], v[16:17]
	v_mov_b64_e32 v[48:49], v[16:17]
	v_mov_b64_e32 v[32:33], v[16:17]
	v_mov_b64_e32 v[62:63], v[14:15]
	v_mov_b64_e32 v[60:61], v[12:13]
	v_mov_b64_e32 v[58:59], v[10:11]
	v_mov_b64_e32 v[56:57], v[8:9]
	v_mov_b64_e32 v[54:55], v[6:7]
	v_mov_b64_e32 v[52:53], v[4:5]
	v_mov_b64_e32 v[50:51], v[2:3]
	v_mov_b64_e32 v[46:47], v[14:15]
	v_mov_b64_e32 v[44:45], v[12:13]
	v_mov_b64_e32 v[42:43], v[10:11]
	v_mov_b64_e32 v[40:41], v[8:9]
	v_mov_b64_e32 v[38:39], v[6:7]
	v_mov_b64_e32 v[36:37], v[4:5]
	v_mov_b64_e32 v[34:35], v[2:3]
	v_mov_b64_e32 v[30:31], v[14:15]
	v_mov_b64_e32 v[28:29], v[12:13]
	v_mov_b64_e32 v[26:27], v[10:11]
	v_mov_b64_e32 v[24:25], v[8:9]
	v_mov_b64_e32 v[22:23], v[6:7]
	v_mov_b64_e32 v[20:21], v[4:5]
	v_mov_b64_e32 v[18:19], v[2:3]
	v_and_b32_e32 v230, 63, v0
	v_lshrrev_b32_e32 v231, 6, v0
	v_lshrrev_b32_e32 v232, 4, v0
	v_mul_u32_u24_e32 v232, 0xe00, v232
	v_and_b32_e32 v233, 15, v0
	v_lshl_add_u32 v232, v233, 4, v232
	v_sub_u32_e32 v232, v186, v232
	v_lshrrev_b32_e32 v233, 3, v0
	v_and_b32_e32 v236, 7, v0
	v_lshlrev_b32_e32 v236, 4, v236
	v_lshl_add_u32 v233, v233, 7, v236
	v_sub_u32_e32 v233, v182, v233
	v_add_u32_e32 v232, 0x39d1dc00, v232
	v_add_u32_e32 v233, 0x39b15600, v233
	v_mov_b32_e32 v243, 0
	v_mov_b32_e32 v244, 0x2000
	v_mov_b32_e32 v245, 0x38000
	v_bfe_u32 v236, v230, 2, 3
	v_lshl_add_u32 v236, v231, 3, v236
	v_and_b32_e32 v237, 0xfffffff3, v236
	v_and_b32_e32 v238, 4, v236
	v_lshl_or_b32 v237, v238, 1, v237
	v_and_b32_e32 v238, 8, v236
	v_lshrrev_b32_e32 v238, 1, v238
	v_or_b32_e32 v237, v237, v238
	v_add_u32_e32 v237, 64, v237
	v_mul_u32_u24_e32 v237, 0xe00, v237
	v_add_u32_e32 v237, v237, v232
	v_lshrrev_b32_e32 v238, 5, v230
	v_lshlrev_b32_e32 v238, 6, v238
	v_and_b32_e32 v239, 3, v230
	v_lshl_add_u32 v238, v239, 4, v238
	v_add_u32_e32 v237, v237, v238
	v_add_u32_e32 v242, 0x100, v237
	v_lshl_add_u64 v[206:207], s[14:15], 0, v[242:243]
	v_mov_b32_e32 v236, v230
	v_mul_u32_u24_e32 v237, 0x2ab, v236
	v_lshrrev_b32_e32 v237, 14, v237
	v_mul_u32_u24_e32 v238, 24, v237
	v_sub_u32_e32 v238, v236, v238
	v_lshl_add_u32 v237, v231, 3, v237
	v_bfe_u32 v239, v237, 1, 3
	v_xor_b32_e32 v238, v238, v239
	v_add_u32_e32 v237, 0x80, v237
	v_mul_u32_u24_e32 v240, 0xe00, v237
	v_add_u32_e32 v240, v240, v232
	v_lshl_add_u32 v240, v238, 4, v240
	v_lshl_add_u32 v241, v237, 7, v233
	v_lshl_add_u32 v241, v238, 4, v241
	v_subrev_u32_e32 v241, 0x100, v241
	v_cmp_gt_u32_e32 vcc, 16, v238
	s_nop 1
	v_cndmask_b32_e32 v242, v241, v240, vcc
	v_cndmask_b32_e32 v205, v244, v245, vcc
	v_lshl_add_u64 v[182:183], s[14:15], 0, v[242:243]
	v_add_u32_e32 v236, 0x40, v230
	v_mul_u32_u24_e32 v237, 0x2ab, v236
	v_lshrrev_b32_e32 v237, 14, v237
	v_mul_u32_u24_e32 v238, 24, v237
	v_sub_u32_e32 v238, v236, v238
	v_lshl_add_u32 v237, v231, 3, v237
	v_bfe_u32 v239, v237, 1, 3
	v_xor_b32_e32 v238, v238, v239
	v_add_u32_e32 v237, 0x80, v237
	v_mul_u32_u24_e32 v240, 0xe00, v237
	v_add_u32_e32 v240, v240, v232
	v_lshl_add_u32 v240, v238, 4, v240
	v_lshl_add_u32 v241, v237, 7, v233
	v_lshl_add_u32 v241, v238, 4, v241
	v_subrev_u32_e32 v241, 0x100, v241
	v_cmp_gt_u32_e32 vcc, 16, v238
	s_nop 1
	v_cndmask_b32_e32 v242, v241, v240, vcc
	v_cndmask_b32_e32 v208, v244, v245, vcc
	v_lshl_add_u64 v[184:185], s[14:15], 0, v[242:243]
	v_add_u32_e32 v236, 0x80, v230
	v_mul_u32_u24_e32 v237, 0x2ab, v236
	v_lshrrev_b32_e32 v237, 14, v237
	v_mul_u32_u24_e32 v238, 24, v237
	v_sub_u32_e32 v238, v236, v238
	v_lshl_add_u32 v237, v231, 3, v237
	v_bfe_u32 v239, v237, 1, 3
	v_xor_b32_e32 v238, v238, v239
	v_add_u32_e32 v237, 0x80, v237
	v_mul_u32_u24_e32 v240, 0xe00, v237
	v_add_u32_e32 v240, v240, v232
	v_lshl_add_u32 v240, v238, 4, v240
	v_lshl_add_u32 v241, v237, 7, v233
	v_lshl_add_u32 v241, v238, 4, v241
	v_subrev_u32_e32 v241, 0x100, v241
	v_cmp_gt_u32_e32 vcc, 16, v238
	s_nop 1
	v_cndmask_b32_e32 v242, v241, v240, vcc
	v_cndmask_b32_e32 v209, v244, v245, vcc
	v_lshl_add_u64 v[186:187], s[14:15], 0, v[242:243]
	v_lshrrev_b32_e32 v236, 8, v0
	s_nop 0
	v_readfirstlane_b32 s98, v236
	s_nop 3
	s_cmp_lg_u32 s98, 0
	s_cbranch_scc0 .Latt_prio_done
	s_setprio 1
.Latt_prio_done:
.LBB0_1344:
	s_cmp_eq_u32 s98, 0
	s_cbranch_scc1 .Latt_p0a
	v_readfirstlane_b32 s4, v0
	s_nop 0
	s_lshl_b32 s5, s4, 4
	s_mul_i32 s4, s5, 3
	s_add_i32 m0, s4, 0x8000
	s_nop 0
	global_load_lds_dwordx4 v[182:183], off
	s_add_i32 m0, s4, 0x8400
	s_nop 0
	global_load_lds_dwordx4 v[184:185], off
	s_add_i32 m0, s4, 0x8800
	s_nop 0
	global_load_lds_dwordx4 v[186:187], off
	s_lshl_b32 s5, s5, 1
	s_add_i32 m0, s5, 0x4000
	s_nop 0
	global_load_lds_dwordx4 v[206:207], off
	s_add_i32 m0, s5, 0x4380
	s_nop 0
	global_load_lds_dwordx4 v[206:207], off offset:128
	v_add_co_u32_e32 v182, vcc, v182, v205
	s_nop 1
	v_addc_co_u32_e32 v183, vcc, 0, v183, vcc
	v_add_co_u32_e32 v184, vcc, v184, v208
	s_nop 1
	v_addc_co_u32_e32 v185, vcc, 0, v185, vcc
	v_add_co_u32_e32 v186, vcc, v186, v209
	s_nop 1
	v_addc_co_u32_e32 v187, vcc, 0, v187, vcc
	v_add_co_u32_e32 v206, vcc, 0x38000, v206
	s_nop 1
	v_addc_co_u32_e32 v207, vcc, 0, v207, vcc
